# speedup vs baseline: 1.0717x; 1.0253x over previous
.LBB0_7:
	s_add_i32 s95, s82, -1
	s_lshl_b32 s90, s91, 6
	s_add_i32 s96, s3, -1
	s_add_i32 s88, s89, s33
	s_cmp_lg_u32 s85, 0
	s_cbranch_scc1 .Litem_loaded
	s_and_saveexec_b64 s[6:7], s[0:1]
	s_cbranch_execz .Lub_skip
	global_load_ubyte v162, v[226:227], off
.Lub_skip:
	s_or_b64 exec, exec, s[6:7]
	v_mov_b32_e32 v2, v0
	s_add_i32 s95, s82, -1
	s_lshl_b32 s90, s91, 6
	v_ashrrev_i32_e32 v52, 4, v2
	v_bfe_u32 v53, v2, 4, 2
	v_lshlrev_b32_e32 v2, 2, v2
	s_cmp_gt_i32 s82, 1
	v_and_or_b32 v2, v2, 60, s90
	s_cselect_b32 s4, 64, 0
	s_add_i32 s96, s3, -1
	v_lshlrev_b64 v[4:5], 2, v[2:3]
	v_min_i32_e32 v2, s96, v52
	v_add_lshl_u32 v2, v2, s76, 10
	v_lshlrev_b64 v[8:9], 2, v[2:3]
	v_add_u32_e32 v2, 32, v52
	v_min_i32_e32 v2, s96, v2
	s_waitcnt lgkmcnt(0)
	v_lshl_add_u64 v[6:7], s[70:71], 0, v[4:5]
	v_add_lshl_u32 v2, v2, s76, 10
	v_lshl_add_u64 v[10:11], v[6:7], 0, v[8:9]
	v_lshlrev_b64 v[12:13], 2, v[2:3]
	v_lshl_add_u64 v[14:15], v[6:7], 0, v[12:13]
	global_load_dwordx4 v[70:73], v[10:11], off
	global_load_dwordx4 v[66:69], v[14:15], off
	v_lshl_add_u64 v[10:11], s[74:75], 0, v[4:5]
	v_lshl_add_u64 v[16:17], v[10:11], 0, v[8:9]
	v_lshl_add_u64 v[50:51], v[10:11], 0, v[12:13]
	global_load_dwordx4 v[182:185], v[16:17], off
	global_load_dwordx4 v[186:189], v[50:51], off
	v_add_u32_e32 v50, s4, v52
	v_min_i32_e32 v2, s96, v50
	v_add_lshl_u32 v2, v2, s76, 10
	v_lshl_add_u64 v[16:17], v[2:3], 2, v[6:7]
	v_add_u32_e32 v2, 32, v50
	v_min_i32_e32 v2, s96, v2
	v_add_lshl_u32 v2, v2, s76, 10
	s_min_i32 s5, s95, 2
	v_lshl_add_u64 v[50:51], v[2:3], 2, v[6:7]
	global_load_dwordx4 v[90:93], v[16:17], off
	global_load_dwordx4 v[82:85], v[50:51], off
	v_lshl_add_u32 v50, s5, 6, v52
	v_min_i32_e32 v2, s96, v50
	v_add_lshl_u32 v2, v2, s76, 10
	v_lshl_add_u64 v[16:17], v[2:3], 2, v[6:7]
	v_add_u32_e32 v2, 32, v50
	v_min_i32_e32 v2, s96, v2
	s_add_i32 s88, s89, s33
	v_add_lshl_u32 v2, v2, s76, 10
	v_add_u32_e32 v54, s88, v53
	v_lshl_add_u64 v[6:7], v[2:3], 2, v[6:7]
	v_min_i32_e32 v2, s96, v54
	v_lshl_add_u64 v[4:5], s[68:69], 0, v[4:5]
	v_add_lshl_u32 v2, v2, s76, 10
	global_load_dwordx4 v[98:101], v[16:17], off
	global_load_dwordx4 v[94:97], v[6:7], off
	v_lshl_add_u64 v[6:7], v[2:3], 2, v[4:5]
	v_add_u32_e32 v2, 4, v54
	v_min_i32_e32 v2, s96, v2
	v_add_lshl_u32 v2, v2, s76, 10
	v_lshl_add_u64 v[16:17], v[2:3], 2, v[4:5]
	v_add_u32_e32 v2, 8, v54
	v_min_i32_e32 v2, s96, v2
	v_add_lshl_u32 v2, v2, s76, 10
	global_load_dwordx4 v[86:89], v[6:7], off sc0 sc1 nt
	global_load_dwordx4 v[74:77], v[16:17], off sc0 sc1 nt
	v_lshl_add_u64 v[6:7], v[2:3], 2, v[4:5]
	v_add_u32_e32 v2, 12, v54
	v_min_i32_e32 v2, s96, v2
	v_add_lshl_u32 v2, v2, s76, 10
	v_lshl_add_u64 v[16:17], v[2:3], 2, v[4:5]
	v_add_u32_e32 v2, 16, v54
	v_min_i32_e32 v2, s96, v2
	v_add_lshl_u32 v2, v2, s76, 10
	global_load_dwordx4 v[78:81], v[6:7], off sc0 sc1 nt
	global_load_dwordx4 v[58:61], v[16:17], off sc0 sc1 nt
	v_lshl_add_u64 v[6:7], v[2:3], 2, v[4:5]
	v_add_u32_e32 v2, 20, v54
	v_min_i32_e32 v2, s96, v2
	v_add_lshl_u32 v2, v2, s76, 10
	v_lshl_add_u64 v[16:17], v[2:3], 2, v[4:5]
	v_add_u32_e32 v2, 24, v54
	v_min_i32_e32 v2, s96, v2
	v_add_lshl_u32 v2, v2, s76, 10
	global_load_dwordx4 v[62:65], v[6:7], off sc0 sc1 nt
	global_load_dwordx4 v[50:53], v[16:17], off sc0 sc1 nt
	v_lshl_add_u64 v[16:17], v[2:3], 2, v[4:5]
	v_add_u32_e32 v2, 28, v54
	v_min_i32_e32 v2, s96, v2
	v_add_lshl_u32 v2, v2, s76, 10
	v_lshl_add_u64 v[102:103], v[2:3], 2, v[4:5]
	global_load_dwordx4 v[54:57], v[16:17], off sc0 sc1 nt
	global_load_dwordx4 v[178:181], v[102:103], off sc0 sc1 nt
.Litem_loaded:
	s_cmp_eq_u32 s85, 0
	s_cselect_b64 s[4:5], -1, 0
	s_and_b64 s[8:9], s[4:5], s[0:1]
	s_and_saveexec_b64 s[6:7], s[8:9]
	s_cbranch_execz .LBB0_11
	s_movk_i32 s8, 0xff
	v_mov_b32_e32 v102, 0
	v_mov_b32_e32 v103, 0
	v_mov_b32_e32 v104, 0
	v_mov_b32_e32 v105, 0
	s_waitcnt vmcnt(16)
	v_mov_b32_e32 v2, v162
	v_cmp_ne_u16_e32 vcc, s8, v2
	s_and_saveexec_b64 s[8:9], vcc
	s_cbranch_execz .LBB0_10
	v_and_b32_sdwa v16, v2, v240 dst_sel:DWORD dst_unused:UNUSED_PAD src0_sel:WORD_0 src1_sel:DWORD
	v_readlane_b32 s16, v255, 0
	v_lshlrev_b32_e32 v16, 2, v16
	v_readlane_b32 s17, v255, 1
	s_nop 4
	global_load_dwordx2 v[102:103], v16, s[16:17]
	v_add_u32_sdwa v16, s2, v2 dst_sel:DWORD dst_unused:UNUSED_PAD src0_sel:DWORD src1_sel:WORD_0
	v_lshlrev_b32_sdwa v2, v241, v2 dst_sel:DWORD dst_unused:UNUSED_PAD src0_sel:DWORD src1_sel:WORD_0
	v_and_or_b32 v16, v16, 7, s67
	v_and_b32_e32 v2, 0xf00, v2
	v_lshl_or_b32 v104, v16, 16, v2
	s_waitcnt vmcnt(0)
	v_sub_u32_e32 v103, v103, v102
	v_add_u32_e32 v2, 63, v103
	v_ashrrev_i32_e32 v16, 31, v2
	v_lshrrev_b32_e32 v16, 26, v16
	v_add_u32_e32 v2, v2, v16
	v_ashrrev_i32_e32 v105, 6, v2
